# epilogue store ladders de-serialised: in straight-line runs the next piece's converts + ds_bpermute exchange are issued before the current piece's wait (lgkmcnt(4)) and store; 77 pieces in the plain G
# speedup vs baseline: 1.0095x; 1.0007x over previous
.LBB0_1215:
	v_lshl_add_u32 v142, s68, 8, v146
	s_lshl_b32 s0, s65, 8
	v_ashrrev_i32_e32 v143, 31, v142
	v_cvt_pk_bf16_f32 v124, v124, v125
	v_cvt_pk_bf16_f32 v125, v126, v127
	v_cvt_pk_bf16_f32 v126, v128, v129
	v_cvt_pk_bf16_f32 v127, v130, v131
	s_ashr_i32 s1, s0, 31
	v_lshlrev_b64 v[148:149], 11, v[142:143]
	ds_bpermute_b32 v124, v145, v124
	ds_bpermute_b32 v125, v145, v125
	ds_bpermute_b32 v126, v145, v126
	ds_bpermute_b32 v127, v145, v127
	v_lshl_add_u64 v[148:149], s[28:29], 0, v[148:149]
	s_lshl_b64 s[0:1], s[0:1], 1
	v_lshl_add_u64 v[128:129], v[148:149], 0, s[0:1]
	s_mov_b32 s65, s11
	v_lshl_add_u64 v[128:129], v[128:129], 0, s[64:65]
	v_lshl_add_u64 v[128:129], v[128:129], 0, v[2:3]
	v_cvt_pk_bf16_f32 v120, v120, v121
	v_cvt_pk_bf16_f32 v121, v122, v123
	v_cvt_pk_bf16_f32 v122, v116, v117
	v_cvt_pk_bf16_f32 v119, v118, v119
	ds_bpermute_b32 v116, v145, v120
	ds_bpermute_b32 v117, v145, v121
	ds_bpermute_b32 v118, v145, v122
	ds_bpermute_b32 v119, v145, v119
	s_waitcnt lgkmcnt(4)
	global_store_dwordx4 v[128:129], v[124:127], off
	s_and_b64 vcc, exec, s[34:35]
	v_cvt_pk_bf16_f32 v112, v112, v113
	v_cvt_pk_bf16_f32 v113, v114, v115
	v_cvt_pk_bf16_f32 v114, v108, v109
	v_cvt_pk_bf16_f32 v111, v110, v111
	ds_bpermute_b32 v108, v145, v112
	ds_bpermute_b32 v109, v145, v113
	ds_bpermute_b32 v110, v145, v114
	ds_bpermute_b32 v111, v145, v111
	s_waitcnt lgkmcnt(4)
	global_store_dwordx4 v[128:129], v[116:119], off offset:256
	s_nop 1
	v_or_b32_e32 v116, 16, v142
	v_ashrrev_i32_e32 v117, 31, v116
	v_lshlrev_b64 v[116:117], 11, v[116:117]
	v_lshl_add_u64 v[112:113], s[28:29], 0, v[116:117]
	v_lshl_add_u64 v[112:113], v[112:113], 0, s[0:1]
	v_lshl_add_u64 v[112:113], v[112:113], 0, s[64:65]
	v_lshl_add_u64 v[112:113], v[112:113], 0, v[2:3]
	v_cvt_pk_bf16_f32 v104, v104, v105
	v_cvt_pk_bf16_f32 v105, v106, v107
	v_cvt_pk_bf16_f32 v106, v100, v101
	v_cvt_pk_bf16_f32 v103, v102, v103
	ds_bpermute_b32 v100, v145, v104
	ds_bpermute_b32 v101, v145, v105
	ds_bpermute_b32 v102, v145, v106
	ds_bpermute_b32 v103, v145, v103
	s_waitcnt lgkmcnt(4)
	global_store_dwordx4 v[112:113], v[108:111], off
	v_cvt_pk_bf16_f32 v96, v96, v97
	v_cvt_pk_bf16_f32 v97, v98, v99
	v_cvt_pk_bf16_f32 v98, v92, v93
	v_cvt_pk_bf16_f32 v95, v94, v95
	ds_bpermute_b32 v92, v145, v96
	ds_bpermute_b32 v93, v145, v97
	ds_bpermute_b32 v94, v145, v98
	ds_bpermute_b32 v95, v145, v95
	s_waitcnt lgkmcnt(4)
	global_store_dwordx4 v[112:113], v[100:103], off offset:256
	s_nop 1
	v_or_b32_e32 v100, 32, v142
	v_ashrrev_i32_e32 v101, 31, v100
	v_lshlrev_b64 v[100:101], 11, v[100:101]
	v_lshl_add_u64 v[96:97], s[28:29], 0, v[100:101]
	v_lshl_add_u64 v[96:97], v[96:97], 0, s[0:1]
	v_lshl_add_u64 v[96:97], v[96:97], 0, s[64:65]
	v_lshl_add_u64 v[96:97], v[96:97], 0, v[2:3]
	v_cvt_pk_bf16_f32 v88, v88, v89
	v_cvt_pk_bf16_f32 v89, v90, v91
	v_cvt_pk_bf16_f32 v90, v84, v85
	v_cvt_pk_bf16_f32 v87, v86, v87
	ds_bpermute_b32 v84, v145, v88
	ds_bpermute_b32 v85, v145, v89
	ds_bpermute_b32 v86, v145, v90
	ds_bpermute_b32 v87, v145, v87
	s_waitcnt lgkmcnt(4)
	global_store_dwordx4 v[96:97], v[92:95], off
	v_cvt_pk_bf16_f32 v80, v80, v81
	v_cvt_pk_bf16_f32 v81, v82, v83
	v_cvt_pk_bf16_f32 v82, v76, v77
	v_cvt_pk_bf16_f32 v79, v78, v79
	ds_bpermute_b32 v76, v145, v80
	ds_bpermute_b32 v77, v145, v81
	ds_bpermute_b32 v78, v145, v82
	ds_bpermute_b32 v79, v145, v79
	s_waitcnt lgkmcnt(4)
	global_store_dwordx4 v[96:97], v[84:87], off offset:256
	s_nop 1
	v_or_b32_e32 v84, 48, v142
	v_ashrrev_i32_e32 v85, 31, v84
	v_lshlrev_b64 v[84:85], 11, v[84:85]
	v_lshl_add_u64 v[80:81], s[28:29], 0, v[84:85]
	v_lshl_add_u64 v[80:81], v[80:81], 0, s[0:1]
	v_lshl_add_u64 v[80:81], v[80:81], 0, s[64:65]
	v_lshl_add_u64 v[80:81], v[80:81], 0, v[2:3]
	v_cvt_pk_bf16_f32 v72, v72, v73
	v_cvt_pk_bf16_f32 v73, v74, v75
	v_cvt_pk_bf16_f32 v74, v68, v69
	v_cvt_pk_bf16_f32 v71, v70, v71
	ds_bpermute_b32 v68, v145, v72
	ds_bpermute_b32 v69, v145, v73
	ds_bpermute_b32 v70, v145, v74
	ds_bpermute_b32 v71, v145, v71
	s_waitcnt lgkmcnt(4)
	global_store_dwordx4 v[80:81], v[76:79], off
	v_cvt_pk_bf16_f32 v64, v64, v65
	v_cvt_pk_bf16_f32 v65, v66, v67
	v_cvt_pk_bf16_f32 v66, v60, v61
	v_cvt_pk_bf16_f32 v63, v62, v63
	ds_bpermute_b32 v60, v145, v64
	ds_bpermute_b32 v61, v145, v65
	ds_bpermute_b32 v62, v145, v66
	ds_bpermute_b32 v63, v145, v63
	s_waitcnt lgkmcnt(4)
	global_store_dwordx4 v[80:81], v[68:71], off offset:256
	s_nop 1
	v_add_u32_e32 v68, 0x80, v142
	v_ashrrev_i32_e32 v69, 31, v68
	v_lshlrev_b64 v[68:69], 11, v[68:69]
	v_lshl_add_u64 v[64:65], s[28:29], 0, v[68:69]
	v_lshl_add_u64 v[64:65], v[64:65], 0, s[0:1]
	v_lshl_add_u64 v[64:65], v[64:65], 0, s[64:65]
	v_lshl_add_u64 v[64:65], v[64:65], 0, v[2:3]
	v_cvt_pk_bf16_f32 v56, v56, v57
	v_cvt_pk_bf16_f32 v57, v58, v59
	v_cvt_pk_bf16_f32 v58, v52, v53
	v_cvt_pk_bf16_f32 v55, v54, v55
	ds_bpermute_b32 v52, v145, v56
	ds_bpermute_b32 v53, v145, v57
	ds_bpermute_b32 v54, v145, v58
	ds_bpermute_b32 v55, v145, v55
	s_waitcnt lgkmcnt(4)
	global_store_dwordx4 v[64:65], v[60:63], off
	v_cvt_pk_bf16_f32 v48, v48, v49
	v_cvt_pk_bf16_f32 v49, v50, v51
	v_cvt_pk_bf16_f32 v50, v44, v45
	v_cvt_pk_bf16_f32 v47, v46, v47
	ds_bpermute_b32 v44, v145, v48
	ds_bpermute_b32 v45, v145, v49
	ds_bpermute_b32 v46, v145, v50
	ds_bpermute_b32 v47, v145, v47
	s_waitcnt lgkmcnt(4)
	global_store_dwordx4 v[64:65], v[52:55], off offset:256
	s_nop 1
	v_add_u32_e32 v52, 0x90, v142
	v_ashrrev_i32_e32 v53, 31, v52
	v_lshlrev_b64 v[52:53], 11, v[52:53]
	v_lshl_add_u64 v[48:49], s[28:29], 0, v[52:53]
	v_lshl_add_u64 v[48:49], v[48:49], 0, s[0:1]
	v_lshl_add_u64 v[48:49], v[48:49], 0, s[64:65]
	v_lshl_add_u64 v[48:49], v[48:49], 0, v[2:3]
	v_cvt_pk_bf16_f32 v40, v40, v41
	v_cvt_pk_bf16_f32 v41, v42, v43
	v_cvt_pk_bf16_f32 v42, v36, v37
	v_cvt_pk_bf16_f32 v39, v38, v39
	ds_bpermute_b32 v36, v145, v40
	ds_bpermute_b32 v37, v145, v41
	ds_bpermute_b32 v38, v145, v42
	ds_bpermute_b32 v39, v145, v39
	s_waitcnt lgkmcnt(4)
	global_store_dwordx4 v[48:49], v[44:47], off
	v_cvt_pk_bf16_f32 v32, v32, v33
	v_cvt_pk_bf16_f32 v33, v34, v35
	v_cvt_pk_bf16_f32 v34, v28, v29
	v_cvt_pk_bf16_f32 v31, v30, v31
	ds_bpermute_b32 v28, v145, v32
	ds_bpermute_b32 v29, v145, v33
	ds_bpermute_b32 v30, v145, v34
	ds_bpermute_b32 v31, v145, v31
	s_waitcnt lgkmcnt(4)
	global_store_dwordx4 v[48:49], v[36:39], off offset:256
	s_nop 1
	v_add_u32_e32 v36, 0xa0, v142
	v_ashrrev_i32_e32 v37, 31, v36
	v_lshlrev_b64 v[36:37], 11, v[36:37]
	v_lshl_add_u64 v[32:33], s[28:29], 0, v[36:37]
	v_lshl_add_u64 v[32:33], v[32:33], 0, s[0:1]
	v_lshl_add_u64 v[32:33], v[32:33], 0, s[64:65]
	v_lshl_add_u64 v[32:33], v[32:33], 0, v[2:3]
	v_cvt_pk_bf16_f32 v24, v24, v25
	v_cvt_pk_bf16_f32 v25, v26, v27
	v_cvt_pk_bf16_f32 v26, v20, v21
	v_cvt_pk_bf16_f32 v23, v22, v23
	ds_bpermute_b32 v20, v145, v24
	ds_bpermute_b32 v21, v145, v25
	ds_bpermute_b32 v22, v145, v26
	ds_bpermute_b32 v23, v145, v23
	s_waitcnt lgkmcnt(4)
	global_store_dwordx4 v[32:33], v[28:31], off
	v_cvt_pk_bf16_f32 v16, v16, v17
	v_cvt_pk_bf16_f32 v17, v18, v19
	v_cvt_pk_bf16_f32 v18, v12, v13
	v_cvt_pk_bf16_f32 v15, v14, v15
	ds_bpermute_b32 v12, v145, v16
	ds_bpermute_b32 v13, v145, v17
	ds_bpermute_b32 v14, v145, v18
	ds_bpermute_b32 v15, v145, v15
	s_waitcnt lgkmcnt(4)
	global_store_dwordx4 v[32:33], v[20:23], off offset:256
	s_nop 1
	v_add_u32_e32 v20, 0xb0, v142
	v_ashrrev_i32_e32 v21, 31, v20
	v_lshlrev_b64 v[20:21], 11, v[20:21]
	v_lshl_add_u64 v[16:17], s[28:29], 0, v[20:21]
	v_lshl_add_u64 v[16:17], v[16:17], 0, s[0:1]
	v_lshl_add_u64 v[16:17], v[16:17], 0, s[64:65]
	v_lshl_add_u64 v[16:17], v[16:17], 0, v[2:3]
	v_cvt_pk_bf16_f32 v8, v8, v9
	v_cvt_pk_bf16_f32 v9, v10, v11
	v_cvt_pk_bf16_f32 v10, v4, v5
	v_cvt_pk_bf16_f32 v7, v6, v7
	ds_bpermute_b32 v4, v145, v8
	ds_bpermute_b32 v5, v145, v9
	ds_bpermute_b32 v6, v145, v10
	ds_bpermute_b32 v7, v145, v7
	s_waitcnt lgkmcnt(4)
	global_store_dwordx4 v[16:17], v[12:15], off
	s_mov_b64 s[0:1], -1
	s_waitcnt lgkmcnt(0)
	global_store_dwordx4 v[16:17], v[4:7], off offset:256
	s_cbranch_vccnz .LBB0_1199
	s_andn2_b64 vcc, exec, s[58:59]
	s_cbranch_vccnz .LBB0_1198
	s_barrier
	s_branch .LBB0_1198

.LBB0_1230:
	v_lshrrev_b32_e32 v0, 2, v140
	v_and_or_b32 v0, v0, 15, s13
	v_and_b32_e32 v2, 3, v140
	v_and_b32_e32 v1, 60, v140
	v_lshl_add_u32 v0, s40, 8, v0
	v_lshl_or_b32 v134, v2, 6, v1
	v_ashrrev_i32_e32 v1, 31, v0
	s_lshl_b32 s0, s23, 9
	v_lshlrev_b64 v[132:133], 11, v[0:1]
	v_cvt_pk_bf16_f32 v1, v128, v129
	v_cvt_pk_bf16_f32 v128, v130, v131
	v_cvt_pk_bf16_f32 v129, v124, v125
	v_cvt_pk_bf16_f32 v127, v126, v127
	s_add_u32 s0, s28, s0
	ds_bpermute_b32 v124, v134, v1
	ds_bpermute_b32 v125, v134, v128
	ds_bpermute_b32 v126, v134, v129
	ds_bpermute_b32 v127, v134, v127
	s_addc_u32 s1, s29, 0
	v_lshl_add_u64 v[132:133], s[0:1], 0, v[132:133]
	s_lshl_b32 s2, s12, 1
	s_mov_b32 s3, s11
	v_lshl_add_u64 v[128:129], v[132:133], 0, s[2:3]
	v_lshlrev_b32_e32 v2, 4, v2
	v_lshl_add_u64 v[128:129], v[128:129], 0, v[2:3]
	v_cvt_pk_bf16_f32 v1, v120, v121
	v_cvt_pk_bf16_f32 v120, v122, v123
	v_cvt_pk_bf16_f32 v121, v116, v117
	v_cvt_pk_bf16_f32 v119, v118, v119
	ds_bpermute_b32 v116, v134, v1
	ds_bpermute_b32 v117, v134, v120
	ds_bpermute_b32 v118, v134, v121
	ds_bpermute_b32 v119, v134, v119
	s_waitcnt lgkmcnt(4)
	global_store_dwordx4 v[128:129], v[124:127], off
	v_cvt_pk_bf16_f32 v1, v112, v113
	v_cvt_pk_bf16_f32 v112, v114, v115
	v_cvt_pk_bf16_f32 v113, v108, v109
	v_cvt_pk_bf16_f32 v111, v110, v111
	ds_bpermute_b32 v108, v134, v1
	ds_bpermute_b32 v109, v134, v112
	ds_bpermute_b32 v110, v134, v113
	ds_bpermute_b32 v111, v134, v111
	s_waitcnt lgkmcnt(4)
	global_store_dwordx4 v[128:129], v[116:119], off offset:256
	s_nop 1
	v_or_b32_e32 v116, 16, v0
	v_ashrrev_i32_e32 v117, 31, v116
	v_lshlrev_b64 v[112:113], 11, v[116:117]
	v_lshl_add_u64 v[112:113], s[0:1], 0, v[112:113]
	v_lshl_add_u64 v[112:113], v[112:113], 0, s[2:3]
	v_lshl_add_u64 v[112:113], v[112:113], 0, v[2:3]
	v_cvt_pk_bf16_f32 v1, v104, v105
	v_cvt_pk_bf16_f32 v104, v106, v107
	v_cvt_pk_bf16_f32 v105, v100, v101
	v_cvt_pk_bf16_f32 v103, v102, v103
	ds_bpermute_b32 v100, v134, v1
	ds_bpermute_b32 v101, v134, v104
	ds_bpermute_b32 v102, v134, v105
	ds_bpermute_b32 v103, v134, v103
	s_waitcnt lgkmcnt(4)
	global_store_dwordx4 v[112:113], v[108:111], off
	v_cvt_pk_bf16_f32 v1, v96, v97
	v_cvt_pk_bf16_f32 v96, v98, v99
	v_cvt_pk_bf16_f32 v97, v92, v93
	v_cvt_pk_bf16_f32 v95, v94, v95
	ds_bpermute_b32 v92, v134, v1
	ds_bpermute_b32 v93, v134, v96
	ds_bpermute_b32 v94, v134, v97
	ds_bpermute_b32 v95, v134, v95
	s_waitcnt lgkmcnt(4)
	global_store_dwordx4 v[112:113], v[100:103], off offset:256
	s_nop 1
	v_or_b32_e32 v100, 32, v0
	v_ashrrev_i32_e32 v101, 31, v100
	v_lshlrev_b64 v[96:97], 11, v[100:101]
	v_lshl_add_u64 v[96:97], s[0:1], 0, v[96:97]
	v_lshl_add_u64 v[96:97], v[96:97], 0, s[2:3]
	v_lshl_add_u64 v[96:97], v[96:97], 0, v[2:3]
	v_cvt_pk_bf16_f32 v1, v88, v89
	v_cvt_pk_bf16_f32 v88, v90, v91
	v_cvt_pk_bf16_f32 v89, v84, v85
	v_cvt_pk_bf16_f32 v87, v86, v87
	ds_bpermute_b32 v84, v134, v1
	ds_bpermute_b32 v85, v134, v88
	ds_bpermute_b32 v86, v134, v89
	ds_bpermute_b32 v87, v134, v87
	s_waitcnt lgkmcnt(4)
	global_store_dwordx4 v[96:97], v[92:95], off
	v_cvt_pk_bf16_f32 v1, v80, v81
	v_cvt_pk_bf16_f32 v80, v82, v83
	v_cvt_pk_bf16_f32 v81, v76, v77
	v_cvt_pk_bf16_f32 v79, v78, v79
	ds_bpermute_b32 v76, v134, v1
	ds_bpermute_b32 v77, v134, v80
	ds_bpermute_b32 v78, v134, v81
	ds_bpermute_b32 v79, v134, v79
	s_waitcnt lgkmcnt(4)
	global_store_dwordx4 v[96:97], v[84:87], off offset:256
	s_nop 1
	v_or_b32_e32 v84, 48, v0
	v_ashrrev_i32_e32 v85, 31, v84
	v_lshlrev_b64 v[80:81], 11, v[84:85]
	v_lshl_add_u64 v[80:81], s[0:1], 0, v[80:81]
	v_lshl_add_u64 v[80:81], v[80:81], 0, s[2:3]
	v_lshl_add_u64 v[80:81], v[80:81], 0, v[2:3]
	v_cvt_pk_bf16_f32 v1, v72, v73
	v_cvt_pk_bf16_f32 v72, v74, v75
	v_cvt_pk_bf16_f32 v73, v68, v69
	v_cvt_pk_bf16_f32 v71, v70, v71
	ds_bpermute_b32 v68, v134, v1
	ds_bpermute_b32 v69, v134, v72
	ds_bpermute_b32 v70, v134, v73
	ds_bpermute_b32 v71, v134, v71
	s_waitcnt lgkmcnt(4)
	global_store_dwordx4 v[80:81], v[76:79], off
	v_cvt_pk_bf16_f32 v1, v64, v65
	v_cvt_pk_bf16_f32 v64, v66, v67
	v_cvt_pk_bf16_f32 v65, v60, v61
	v_cvt_pk_bf16_f32 v63, v62, v63
	ds_bpermute_b32 v60, v134, v1
	ds_bpermute_b32 v61, v134, v64
	ds_bpermute_b32 v62, v134, v65
	ds_bpermute_b32 v63, v134, v63
	s_waitcnt lgkmcnt(4)
	global_store_dwordx4 v[80:81], v[68:71], off offset:256
	s_nop 1
	v_add_u32_e32 v68, 0x80, v0
	v_ashrrev_i32_e32 v69, 31, v68
	v_lshlrev_b64 v[64:65], 11, v[68:69]
	v_lshl_add_u64 v[64:65], s[0:1], 0, v[64:65]
	v_lshl_add_u64 v[64:65], v[64:65], 0, s[2:3]
	v_lshl_add_u64 v[64:65], v[64:65], 0, v[2:3]
	v_cvt_pk_bf16_f32 v1, v56, v57
	v_cvt_pk_bf16_f32 v56, v58, v59
	v_cvt_pk_bf16_f32 v57, v52, v53
	v_cvt_pk_bf16_f32 v55, v54, v55
	ds_bpermute_b32 v52, v134, v1
	ds_bpermute_b32 v53, v134, v56
	ds_bpermute_b32 v54, v134, v57
	ds_bpermute_b32 v55, v134, v55
	s_waitcnt lgkmcnt(4)
	global_store_dwordx4 v[64:65], v[60:63], off
	v_cvt_pk_bf16_f32 v1, v48, v49
	v_cvt_pk_bf16_f32 v48, v50, v51
	v_cvt_pk_bf16_f32 v49, v44, v45
	v_cvt_pk_bf16_f32 v47, v46, v47
	ds_bpermute_b32 v44, v134, v1
	ds_bpermute_b32 v45, v134, v48
	ds_bpermute_b32 v46, v134, v49
	ds_bpermute_b32 v47, v134, v47
	s_waitcnt lgkmcnt(4)
	global_store_dwordx4 v[64:65], v[52:55], off offset:256
	s_nop 1
	v_add_u32_e32 v52, 0x90, v0
	v_ashrrev_i32_e32 v53, 31, v52
	v_lshlrev_b64 v[48:49], 11, v[52:53]
	v_lshl_add_u64 v[48:49], s[0:1], 0, v[48:49]
	v_lshl_add_u64 v[48:49], v[48:49], 0, s[2:3]
	v_lshl_add_u64 v[48:49], v[48:49], 0, v[2:3]
	v_cvt_pk_bf16_f32 v1, v40, v41
	v_cvt_pk_bf16_f32 v40, v42, v43
	v_cvt_pk_bf16_f32 v41, v36, v37
	v_cvt_pk_bf16_f32 v39, v38, v39
	ds_bpermute_b32 v36, v134, v1
	ds_bpermute_b32 v37, v134, v40
	ds_bpermute_b32 v38, v134, v41
	ds_bpermute_b32 v39, v134, v39
	s_waitcnt lgkmcnt(4)
	global_store_dwordx4 v[48:49], v[44:47], off
	v_cvt_pk_bf16_f32 v1, v32, v33
	v_cvt_pk_bf16_f32 v32, v34, v35
	v_cvt_pk_bf16_f32 v33, v28, v29
	v_cvt_pk_bf16_f32 v31, v30, v31
	ds_bpermute_b32 v28, v134, v1
	ds_bpermute_b32 v29, v134, v32
	ds_bpermute_b32 v30, v134, v33
	ds_bpermute_b32 v31, v134, v31
	s_waitcnt lgkmcnt(4)
	global_store_dwordx4 v[48:49], v[36:39], off offset:256
	s_nop 1
	v_add_u32_e32 v36, 0xa0, v0
	v_ashrrev_i32_e32 v37, 31, v36
	v_lshlrev_b64 v[32:33], 11, v[36:37]
	v_lshl_add_u64 v[32:33], s[0:1], 0, v[32:33]
	v_lshl_add_u64 v[32:33], v[32:33], 0, s[2:3]
	v_lshl_add_u64 v[32:33], v[32:33], 0, v[2:3]
	v_cvt_pk_bf16_f32 v1, v24, v25
	v_cvt_pk_bf16_f32 v24, v26, v27
	v_cvt_pk_bf16_f32 v25, v20, v21
	v_cvt_pk_bf16_f32 v23, v22, v23
	ds_bpermute_b32 v20, v134, v1
	ds_bpermute_b32 v21, v134, v24
	ds_bpermute_b32 v22, v134, v25
	ds_bpermute_b32 v23, v134, v23
	s_waitcnt lgkmcnt(4)
	global_store_dwordx4 v[32:33], v[28:31], off
	v_add_u32_e32 v0, 0xb0, v0
	v_ashrrev_i32_e32 v1, 31, v0
	v_lshlrev_b64 v[0:1], 11, v[0:1]
	v_lshl_add_u64 v[0:1], s[0:1], 0, v[0:1]
	v_cvt_pk_bf16_f32 v16, v16, v17
	v_cvt_pk_bf16_f32 v17, v18, v19
	v_cvt_pk_bf16_f32 v18, v12, v13
	v_cvt_pk_bf16_f32 v15, v14, v15
	ds_bpermute_b32 v12, v134, v16
	ds_bpermute_b32 v13, v134, v17
	ds_bpermute_b32 v14, v134, v18
	ds_bpermute_b32 v15, v134, v15
	s_waitcnt lgkmcnt(4)
	global_store_dwordx4 v[32:33], v[20:23], off offset:256
	v_lshl_add_u64 v[0:1], v[0:1], 0, s[2:3]
	v_lshl_add_u64 v[0:1], v[0:1], 0, v[2:3]
	v_cvt_pk_bf16_f32 v2, v8, v9
	v_cvt_pk_bf16_f32 v8, v10, v11
	v_cvt_pk_bf16_f32 v9, v4, v5
	v_cvt_pk_bf16_f32 v7, v6, v7
	ds_bpermute_b32 v4, v134, v2
	ds_bpermute_b32 v5, v134, v8
	ds_bpermute_b32 v6, v134, v9
	ds_bpermute_b32 v7, v134, v7
	s_waitcnt lgkmcnt(4)
	global_store_dwordx4 v[0:1], v[12:15], off
	s_waitcnt lgkmcnt(0)
	global_store_dwordx4 v[0:1], v[4:7], off offset:256
	s_waitcnt vmcnt(0)
	s_barrier

.LBB0_2146:
	v_lshl_add_u32 v142, s50, 8, v146
	s_lshl_b32 s0, s47, 8
	v_ashrrev_i32_e32 v143, 31, v142
	v_cvt_pk_bf16_f32 v124, v124, v125
	v_cvt_pk_bf16_f32 v125, v126, v127
	v_cvt_pk_bf16_f32 v126, v128, v129
	v_cvt_pk_bf16_f32 v127, v130, v131
	s_ashr_i32 s1, s0, 31
	v_lshlrev_b64 v[148:149], 11, v[142:143]
	ds_bpermute_b32 v124, v145, v124
	ds_bpermute_b32 v125, v145, v125
	ds_bpermute_b32 v126, v145, v126
	ds_bpermute_b32 v127, v145, v127
	v_lshl_add_u64 v[148:149], s[40:41], 0, v[148:149]
	s_lshl_b64 s[0:1], s[0:1], 1
	v_lshl_add_u64 v[128:129], v[148:149], 0, s[0:1]
	s_mov_b32 s47, s11
	v_lshl_add_u64 v[128:129], v[128:129], 0, s[46:47]
	v_lshl_add_u64 v[128:129], v[128:129], 0, v[2:3]
	v_cvt_pk_bf16_f32 v120, v120, v121
	v_cvt_pk_bf16_f32 v121, v122, v123
	v_cvt_pk_bf16_f32 v122, v116, v117
	v_cvt_pk_bf16_f32 v119, v118, v119
	ds_bpermute_b32 v116, v145, v120
	ds_bpermute_b32 v117, v145, v121
	ds_bpermute_b32 v118, v145, v122
	ds_bpermute_b32 v119, v145, v119
	s_waitcnt lgkmcnt(4)
	global_store_dwordx4 v[128:129], v[124:127], off
	s_and_b64 vcc, exec, s[34:35]
	v_cvt_pk_bf16_f32 v112, v112, v113
	v_cvt_pk_bf16_f32 v113, v114, v115
	v_cvt_pk_bf16_f32 v114, v108, v109
	v_cvt_pk_bf16_f32 v111, v110, v111
	ds_bpermute_b32 v108, v145, v112
	ds_bpermute_b32 v109, v145, v113
	ds_bpermute_b32 v110, v145, v114
	ds_bpermute_b32 v111, v145, v111
	s_waitcnt lgkmcnt(4)
	global_store_dwordx4 v[128:129], v[116:119], off offset:256
	s_nop 1
	v_or_b32_e32 v116, 16, v142
	v_ashrrev_i32_e32 v117, 31, v116
	v_lshlrev_b64 v[116:117], 11, v[116:117]
	v_lshl_add_u64 v[112:113], s[40:41], 0, v[116:117]
	v_lshl_add_u64 v[112:113], v[112:113], 0, s[0:1]
	v_lshl_add_u64 v[112:113], v[112:113], 0, s[46:47]
	v_lshl_add_u64 v[112:113], v[112:113], 0, v[2:3]
	v_cvt_pk_bf16_f32 v104, v104, v105
	v_cvt_pk_bf16_f32 v105, v106, v107
	v_cvt_pk_bf16_f32 v106, v100, v101
	v_cvt_pk_bf16_f32 v103, v102, v103
	ds_bpermute_b32 v100, v145, v104
	ds_bpermute_b32 v101, v145, v105
	ds_bpermute_b32 v102, v145, v106
	ds_bpermute_b32 v103, v145, v103
	s_waitcnt lgkmcnt(4)
	global_store_dwordx4 v[112:113], v[108:111], off
	v_cvt_pk_bf16_f32 v96, v96, v97
	v_cvt_pk_bf16_f32 v97, v98, v99
	v_cvt_pk_bf16_f32 v98, v92, v93
	v_cvt_pk_bf16_f32 v95, v94, v95
	ds_bpermute_b32 v92, v145, v96
	ds_bpermute_b32 v93, v145, v97
	ds_bpermute_b32 v94, v145, v98
	ds_bpermute_b32 v95, v145, v95
	s_waitcnt lgkmcnt(4)
	global_store_dwordx4 v[112:113], v[100:103], off offset:256
	s_nop 1
	v_or_b32_e32 v100, 32, v142
	v_ashrrev_i32_e32 v101, 31, v100
	v_lshlrev_b64 v[100:101], 11, v[100:101]
	v_lshl_add_u64 v[96:97], s[40:41], 0, v[100:101]
	v_lshl_add_u64 v[96:97], v[96:97], 0, s[0:1]
	v_lshl_add_u64 v[96:97], v[96:97], 0, s[46:47]
	v_lshl_add_u64 v[96:97], v[96:97], 0, v[2:3]
	v_cvt_pk_bf16_f32 v88, v88, v89
	v_cvt_pk_bf16_f32 v89, v90, v91
	v_cvt_pk_bf16_f32 v90, v84, v85
	v_cvt_pk_bf16_f32 v87, v86, v87
	ds_bpermute_b32 v84, v145, v88
	ds_bpermute_b32 v85, v145, v89
	ds_bpermute_b32 v86, v145, v90
	ds_bpermute_b32 v87, v145, v87
	s_waitcnt lgkmcnt(4)
	global_store_dwordx4 v[96:97], v[92:95], off
	v_cvt_pk_bf16_f32 v80, v80, v81
	v_cvt_pk_bf16_f32 v81, v82, v83
	v_cvt_pk_bf16_f32 v82, v76, v77
	v_cvt_pk_bf16_f32 v79, v78, v79
	ds_bpermute_b32 v76, v145, v80
	ds_bpermute_b32 v77, v145, v81
	ds_bpermute_b32 v78, v145, v82
	ds_bpermute_b32 v79, v145, v79
	s_waitcnt lgkmcnt(4)
	global_store_dwordx4 v[96:97], v[84:87], off offset:256
	s_nop 1
	v_or_b32_e32 v84, 48, v142
	v_ashrrev_i32_e32 v85, 31, v84
	v_lshlrev_b64 v[84:85], 11, v[84:85]
	v_lshl_add_u64 v[80:81], s[40:41], 0, v[84:85]
	v_lshl_add_u64 v[80:81], v[80:81], 0, s[0:1]
	v_lshl_add_u64 v[80:81], v[80:81], 0, s[46:47]
	v_lshl_add_u64 v[80:81], v[80:81], 0, v[2:3]
	v_cvt_pk_bf16_f32 v72, v72, v73
	v_cvt_pk_bf16_f32 v73, v74, v75
	v_cvt_pk_bf16_f32 v74, v68, v69
	v_cvt_pk_bf16_f32 v71, v70, v71
	ds_bpermute_b32 v68, v145, v72
	ds_bpermute_b32 v69, v145, v73
	ds_bpermute_b32 v70, v145, v74
	ds_bpermute_b32 v71, v145, v71
	s_waitcnt lgkmcnt(4)
	global_store_dwordx4 v[80:81], v[76:79], off
	v_cvt_pk_bf16_f32 v64, v64, v65
	v_cvt_pk_bf16_f32 v65, v66, v67
	v_cvt_pk_bf16_f32 v66, v60, v61
	v_cvt_pk_bf16_f32 v63, v62, v63
	ds_bpermute_b32 v60, v145, v64
	ds_bpermute_b32 v61, v145, v65
	ds_bpermute_b32 v62, v145, v66
	ds_bpermute_b32 v63, v145, v63
	s_waitcnt lgkmcnt(4)
	global_store_dwordx4 v[80:81], v[68:71], off offset:256
	s_nop 1
	v_add_u32_e32 v68, 0x80, v142
	v_ashrrev_i32_e32 v69, 31, v68
	v_lshlrev_b64 v[68:69], 11, v[68:69]
	v_lshl_add_u64 v[64:65], s[40:41], 0, v[68:69]
	v_lshl_add_u64 v[64:65], v[64:65], 0, s[0:1]
	v_lshl_add_u64 v[64:65], v[64:65], 0, s[46:47]
	v_lshl_add_u64 v[64:65], v[64:65], 0, v[2:3]
	v_cvt_pk_bf16_f32 v56, v56, v57
	v_cvt_pk_bf16_f32 v57, v58, v59
	v_cvt_pk_bf16_f32 v58, v52, v53
	v_cvt_pk_bf16_f32 v55, v54, v55
	ds_bpermute_b32 v52, v145, v56
	ds_bpermute_b32 v53, v145, v57
	ds_bpermute_b32 v54, v145, v58
	ds_bpermute_b32 v55, v145, v55
	s_waitcnt lgkmcnt(4)
	global_store_dwordx4 v[64:65], v[60:63], off
	v_cvt_pk_bf16_f32 v48, v48, v49
	v_cvt_pk_bf16_f32 v49, v50, v51
	v_cvt_pk_bf16_f32 v50, v44, v45
	v_cvt_pk_bf16_f32 v47, v46, v47
	ds_bpermute_b32 v44, v145, v48
	ds_bpermute_b32 v45, v145, v49
	ds_bpermute_b32 v46, v145, v50
	ds_bpermute_b32 v47, v145, v47
	s_waitcnt lgkmcnt(4)
	global_store_dwordx4 v[64:65], v[52:55], off offset:256
	s_nop 1
	v_add_u32_e32 v52, 0x90, v142
	v_ashrrev_i32_e32 v53, 31, v52
	v_lshlrev_b64 v[52:53], 11, v[52:53]
	v_lshl_add_u64 v[48:49], s[40:41], 0, v[52:53]
	v_lshl_add_u64 v[48:49], v[48:49], 0, s[0:1]
	v_lshl_add_u64 v[48:49], v[48:49], 0, s[46:47]
	v_lshl_add_u64 v[48:49], v[48:49], 0, v[2:3]
	v_cvt_pk_bf16_f32 v40, v40, v41
	v_cvt_pk_bf16_f32 v41, v42, v43
	v_cvt_pk_bf16_f32 v42, v36, v37
	v_cvt_pk_bf16_f32 v39, v38, v39
	ds_bpermute_b32 v36, v145, v40
	ds_bpermute_b32 v37, v145, v41
	ds_bpermute_b32 v38, v145, v42
	ds_bpermute_b32 v39, v145, v39
	s_waitcnt lgkmcnt(4)
	global_store_dwordx4 v[48:49], v[44:47], off
	v_cvt_pk_bf16_f32 v32, v32, v33
	v_cvt_pk_bf16_f32 v33, v34, v35
	v_cvt_pk_bf16_f32 v34, v28, v29
	v_cvt_pk_bf16_f32 v31, v30, v31
	ds_bpermute_b32 v28, v145, v32
	ds_bpermute_b32 v29, v145, v33
	ds_bpermute_b32 v30, v145, v34
	ds_bpermute_b32 v31, v145, v31
	s_waitcnt lgkmcnt(4)
	global_store_dwordx4 v[48:49], v[36:39], off offset:256
	s_nop 1
	v_add_u32_e32 v36, 0xa0, v142
	v_ashrrev_i32_e32 v37, 31, v36
	v_lshlrev_b64 v[36:37], 11, v[36:37]
	v_lshl_add_u64 v[32:33], s[40:41], 0, v[36:37]
	v_lshl_add_u64 v[32:33], v[32:33], 0, s[0:1]
	v_lshl_add_u64 v[32:33], v[32:33], 0, s[46:47]
	v_lshl_add_u64 v[32:33], v[32:33], 0, v[2:3]
	v_cvt_pk_bf16_f32 v24, v24, v25
	v_cvt_pk_bf16_f32 v25, v26, v27
	v_cvt_pk_bf16_f32 v26, v20, v21
	v_cvt_pk_bf16_f32 v23, v22, v23
	ds_bpermute_b32 v20, v145, v24
	ds_bpermute_b32 v21, v145, v25
	ds_bpermute_b32 v22, v145, v26
	ds_bpermute_b32 v23, v145, v23
	s_waitcnt lgkmcnt(4)
	global_store_dwordx4 v[32:33], v[28:31], off
	v_cvt_pk_bf16_f32 v16, v16, v17
	v_cvt_pk_bf16_f32 v17, v18, v19
	v_cvt_pk_bf16_f32 v18, v12, v13
	v_cvt_pk_bf16_f32 v15, v14, v15
	ds_bpermute_b32 v12, v145, v16
	ds_bpermute_b32 v13, v145, v17
	ds_bpermute_b32 v14, v145, v18
	ds_bpermute_b32 v15, v145, v15
	s_waitcnt lgkmcnt(4)
	global_store_dwordx4 v[32:33], v[20:23], off offset:256
	s_nop 1
	v_add_u32_e32 v20, 0xb0, v142
	v_ashrrev_i32_e32 v21, 31, v20
	v_lshlrev_b64 v[20:21], 11, v[20:21]
	v_lshl_add_u64 v[16:17], s[40:41], 0, v[20:21]
	v_lshl_add_u64 v[16:17], v[16:17], 0, s[0:1]
	v_lshl_add_u64 v[16:17], v[16:17], 0, s[46:47]
	v_lshl_add_u64 v[16:17], v[16:17], 0, v[2:3]
	v_cvt_pk_bf16_f32 v8, v8, v9
	v_cvt_pk_bf16_f32 v9, v10, v11
	v_cvt_pk_bf16_f32 v10, v4, v5
	v_cvt_pk_bf16_f32 v7, v6, v7
	ds_bpermute_b32 v4, v145, v8
	ds_bpermute_b32 v5, v145, v9
	ds_bpermute_b32 v6, v145, v10
	ds_bpermute_b32 v7, v145, v7
	s_waitcnt lgkmcnt(4)
	global_store_dwordx4 v[16:17], v[12:15], off
	s_mov_b64 s[0:1], -1
	s_waitcnt lgkmcnt(0)
	global_store_dwordx4 v[16:17], v[4:7], off offset:256
	s_cbranch_vccnz .LBB0_2130
	s_andn2_b64 vcc, exec, s[38:39]
	s_cbranch_vccnz .LBB0_2129
	s_barrier
	s_branch .LBB0_2129

.LBB0_2316:
	v_lshl_add_u32 v20, s50, 8, v152
	v_ashrrev_i32_e32 v21, 31, v20
	s_lshl_b32 s0, s47, 8
	v_lshlrev_b64 v[22:23], 10, v[20:21]
	v_cvt_pk_bf16_f32 v21, v128, v129
	v_cvt_pk_bf16_f32 v29, v130, v131
	v_cvt_pk_bf16_f32 v30, v124, v125
	v_cvt_pk_bf16_f32 v31, v126, v127
	s_ashr_i32 s1, s0, 31
	ds_bpermute_b32 v28, v151, v21
	ds_bpermute_b32 v29, v151, v29
	ds_bpermute_b32 v30, v151, v30
	ds_bpermute_b32 v31, v151, v31
	v_lshl_add_u64 v[22:23], s[40:41], 0, v[22:23]
	s_lshl_b64 s[0:1], s[0:1], 1
	v_lshl_add_u64 v[22:23], v[22:23], 0, s[0:1]
	s_mov_b32 s47, s11
	v_lshl_add_u64 v[22:23], v[22:23], 0, s[46:47]
	v_lshl_add_u64 v[22:23], v[22:23], 0, v[2:3]
	s_waitcnt lgkmcnt(0)
	global_store_dwordx4 v[22:23], v[28:31], off
	v_cvt_pk_bf16_f32 v21, v144, v145
	ds_bpermute_b32 v28, v151, v21
	s_and_b64 vcc, exec, s[34:35]
	v_cvt_pk_bf16_f32 v29, v142, v143
	v_cvt_pk_bf16_f32 v30, v148, v149
	v_cvt_pk_bf16_f32 v31, v146, v147
	ds_bpermute_b32 v29, v151, v29
	ds_bpermute_b32 v30, v151, v30
	ds_bpermute_b32 v31, v151, v31
	s_waitcnt lgkmcnt(0)
	global_store_dwordx4 v[22:23], v[28:31], off offset:256
	v_or_b32_e32 v22, 16, v20
	v_ashrrev_i32_e32 v23, 31, v22
	v_cvt_pk_bf16_f32 v21, v106, v107
	v_cvt_pk_bf16_f32 v29, v104, v105
	v_cvt_pk_bf16_f32 v30, v114, v115
	v_cvt_pk_bf16_f32 v31, v112, v113
	v_lshlrev_b64 v[22:23], 10, v[22:23]
	ds_bpermute_b32 v28, v151, v21
	ds_bpermute_b32 v29, v151, v29
	ds_bpermute_b32 v30, v151, v30
	ds_bpermute_b32 v31, v151, v31
	v_lshl_add_u64 v[22:23], s[40:41], 0, v[22:23]
	v_lshl_add_u64 v[22:23], v[22:23], 0, s[0:1]
	v_lshl_add_u64 v[22:23], v[22:23], 0, s[46:47]
	v_lshl_add_u64 v[22:23], v[22:23], 0, v[2:3]
	s_waitcnt lgkmcnt(0)
	global_store_dwordx4 v[22:23], v[28:31], off
	v_cvt_pk_bf16_f32 v21, v118, v119
	ds_bpermute_b32 v28, v151, v21
	s_nop 0
	v_cvt_pk_bf16_f32 v29, v116, v117
	v_cvt_pk_bf16_f32 v30, v122, v123
	v_cvt_pk_bf16_f32 v31, v120, v121
	ds_bpermute_b32 v29, v151, v29
	ds_bpermute_b32 v30, v151, v30
	ds_bpermute_b32 v31, v151, v31
	s_waitcnt lgkmcnt(0)
	global_store_dwordx4 v[22:23], v[28:31], off offset:256
	v_or_b32_e32 v22, 32, v20
	v_ashrrev_i32_e32 v23, 31, v22
	v_cvt_pk_bf16_f32 v21, v90, v91
	v_cvt_pk_bf16_f32 v29, v88, v89
	v_cvt_pk_bf16_f32 v30, v98, v99
	v_cvt_pk_bf16_f32 v31, v96, v97
	v_lshlrev_b64 v[22:23], 10, v[22:23]
	ds_bpermute_b32 v28, v151, v21
	ds_bpermute_b32 v29, v151, v29
	ds_bpermute_b32 v30, v151, v30
	ds_bpermute_b32 v31, v151, v31
	v_lshl_add_u64 v[22:23], s[40:41], 0, v[22:23]
	v_lshl_add_u64 v[22:23], v[22:23], 0, s[0:1]
	v_lshl_add_u64 v[22:23], v[22:23], 0, s[46:47]
	v_lshl_add_u64 v[22:23], v[22:23], 0, v[2:3]
	s_waitcnt lgkmcnt(0)
	global_store_dwordx4 v[22:23], v[28:31], off
	v_cvt_pk_bf16_f32 v21, v102, v103
	ds_bpermute_b32 v28, v151, v21
	s_nop 0
	v_cvt_pk_bf16_f32 v29, v100, v101
	v_cvt_pk_bf16_f32 v30, v110, v111
	v_cvt_pk_bf16_f32 v31, v108, v109
	ds_bpermute_b32 v29, v151, v29
	ds_bpermute_b32 v30, v151, v30
	ds_bpermute_b32 v31, v151, v31
	s_waitcnt lgkmcnt(0)
	global_store_dwordx4 v[22:23], v[28:31], off offset:256
	v_or_b32_e32 v22, 48, v20
	v_ashrrev_i32_e32 v23, 31, v22
	v_cvt_pk_bf16_f32 v21, v78, v79
	v_cvt_pk_bf16_f32 v29, v76, v77
	v_cvt_pk_bf16_f32 v30, v82, v83
	v_cvt_pk_bf16_f32 v31, v80, v81
	v_lshlrev_b64 v[22:23], 10, v[22:23]
	ds_bpermute_b32 v28, v151, v21
	ds_bpermute_b32 v29, v151, v29
	ds_bpermute_b32 v30, v151, v30
	ds_bpermute_b32 v31, v151, v31
	v_lshl_add_u64 v[22:23], s[40:41], 0, v[22:23]
	v_lshl_add_u64 v[22:23], v[22:23], 0, s[0:1]
	v_lshl_add_u64 v[22:23], v[22:23], 0, s[46:47]
	v_lshl_add_u64 v[22:23], v[22:23], 0, v[2:3]
	s_waitcnt lgkmcnt(0)
	global_store_dwordx4 v[22:23], v[28:31], off
	v_cvt_pk_bf16_f32 v21, v72, v73
	ds_bpermute_b32 v28, v151, v21
	s_nop 0
	v_cvt_pk_bf16_f32 v29, v74, v75
	v_cvt_pk_bf16_f32 v30, v68, v69
	v_cvt_pk_bf16_f32 v31, v70, v71
	ds_bpermute_b32 v29, v151, v29
	ds_bpermute_b32 v30, v151, v30
	ds_bpermute_b32 v31, v151, v31
	s_waitcnt lgkmcnt(0)
	global_store_dwordx4 v[22:23], v[28:31], off offset:256
	v_add_u32_e32 v22, 0x80, v20
	v_ashrrev_i32_e32 v23, 31, v22
	v_cvt_pk_bf16_f32 v21, v64, v65
	v_cvt_pk_bf16_f32 v29, v66, v67
	v_cvt_pk_bf16_f32 v30, v60, v61
	v_cvt_pk_bf16_f32 v31, v62, v63
	v_lshlrev_b64 v[22:23], 10, v[22:23]
	ds_bpermute_b32 v28, v151, v21
	ds_bpermute_b32 v29, v151, v29
	ds_bpermute_b32 v30, v151, v30
	ds_bpermute_b32 v31, v151, v31
	v_lshl_add_u64 v[22:23], s[40:41], 0, v[22:23]
	v_lshl_add_u64 v[22:23], v[22:23], 0, s[0:1]
	v_lshl_add_u64 v[22:23], v[22:23], 0, s[46:47]
	v_lshl_add_u64 v[22:23], v[22:23], 0, v[2:3]
	s_waitcnt lgkmcnt(0)
	global_store_dwordx4 v[22:23], v[28:31], off
	v_cvt_pk_bf16_f32 v21, v86, v87
	ds_bpermute_b32 v28, v151, v21
	s_nop 0
	v_cvt_pk_bf16_f32 v29, v84, v85
	v_cvt_pk_bf16_f32 v30, v94, v95
	v_cvt_pk_bf16_f32 v31, v92, v93
	ds_bpermute_b32 v29, v151, v29
	ds_bpermute_b32 v30, v151, v30
	ds_bpermute_b32 v31, v151, v31
	s_waitcnt lgkmcnt(0)
	global_store_dwordx4 v[22:23], v[28:31], off offset:256
	v_add_u32_e32 v22, 0x90, v20
	v_ashrrev_i32_e32 v23, 31, v22
	v_cvt_pk_bf16_f32 v21, v42, v43
	v_cvt_pk_bf16_f32 v29, v40, v41
	v_cvt_pk_bf16_f32 v30, v50, v51
	v_cvt_pk_bf16_f32 v31, v48, v49
	v_lshlrev_b64 v[22:23], 10, v[22:23]
	ds_bpermute_b32 v28, v151, v21
	ds_bpermute_b32 v29, v151, v29
	ds_bpermute_b32 v30, v151, v30
	ds_bpermute_b32 v31, v151, v31
	v_lshl_add_u64 v[22:23], s[40:41], 0, v[22:23]
	v_lshl_add_u64 v[22:23], v[22:23], 0, s[0:1]
	v_lshl_add_u64 v[22:23], v[22:23], 0, s[46:47]
	v_lshl_add_u64 v[22:23], v[22:23], 0, v[2:3]
	s_waitcnt lgkmcnt(0)
	global_store_dwordx4 v[22:23], v[28:31], off
	v_cvt_pk_bf16_f32 v21, v54, v55
	ds_bpermute_b32 v28, v151, v21
	s_nop 0
	v_cvt_pk_bf16_f32 v29, v52, v53
	v_cvt_pk_bf16_f32 v30, v58, v59
	v_cvt_pk_bf16_f32 v31, v56, v57
	ds_bpermute_b32 v29, v151, v29
	ds_bpermute_b32 v30, v151, v30
	ds_bpermute_b32 v31, v151, v31
	s_waitcnt lgkmcnt(0)
	global_store_dwordx4 v[22:23], v[28:31], off offset:256
	v_add_u32_e32 v22, 0xa0, v20
	v_ashrrev_i32_e32 v23, 31, v22
	v_lshlrev_b64 v[28:29], 10, v[22:23]
	v_cvt_pk_bf16_f32 v21, v26, v27
	v_cvt_pk_bf16_f32 v23, v24, v25
	v_cvt_pk_bf16_f32 v24, v34, v35
	v_cvt_pk_bf16_f32 v25, v32, v33
	ds_bpermute_b32 v22, v151, v21
	ds_bpermute_b32 v23, v151, v23
	ds_bpermute_b32 v24, v151, v24
	ds_bpermute_b32 v25, v151, v25
	v_lshl_add_u64 v[26:27], s[40:41], 0, v[28:29]
	v_lshl_add_u64 v[26:27], v[26:27], 0, s[0:1]
	v_lshl_add_u64 v[26:27], v[26:27], 0, s[46:47]
	v_lshl_add_u64 v[26:27], v[26:27], 0, v[2:3]
	s_waitcnt lgkmcnt(0)
	global_store_dwordx4 v[26:27], v[22:25], off
	v_cvt_pk_bf16_f32 v21, v38, v39
	ds_bpermute_b32 v22, v151, v21
	v_add_u32_e32 v20, 0xb0, v20
	v_cvt_pk_bf16_f32 v23, v36, v37
	v_cvt_pk_bf16_f32 v24, v46, v47
	v_cvt_pk_bf16_f32 v25, v44, v45
	ds_bpermute_b32 v23, v151, v23
	ds_bpermute_b32 v24, v151, v24
	ds_bpermute_b32 v25, v151, v25
	v_ashrrev_i32_e32 v21, 31, v20
	v_lshlrev_b64 v[20:21], 10, v[20:21]
	v_cvt_pk_bf16_f32 v14, v14, v15
	v_cvt_pk_bf16_f32 v13, v12, v13
	v_cvt_pk_bf16_f32 v15, v18, v19
	v_cvt_pk_bf16_f32 v16, v16, v17
	ds_bpermute_b32 v12, v151, v14
	ds_bpermute_b32 v13, v151, v13
	ds_bpermute_b32 v14, v151, v15
	ds_bpermute_b32 v15, v151, v16
	s_waitcnt lgkmcnt(4)
	global_store_dwordx4 v[26:27], v[22:25], off offset:256
	v_lshl_add_u64 v[16:17], s[40:41], 0, v[20:21]
	v_lshl_add_u64 v[16:17], v[16:17], 0, s[0:1]
	v_lshl_add_u64 v[16:17], v[16:17], 0, s[46:47]
	v_lshl_add_u64 v[16:17], v[16:17], 0, v[2:3]
	v_cvt_pk_bf16_f32 v8, v8, v9
	v_cvt_pk_bf16_f32 v9, v10, v11
	v_cvt_pk_bf16_f32 v10, v4, v5
	v_cvt_pk_bf16_f32 v7, v6, v7
	ds_bpermute_b32 v4, v151, v8
	ds_bpermute_b32 v5, v151, v9
	ds_bpermute_b32 v6, v151, v10
	ds_bpermute_b32 v7, v151, v7
	s_waitcnt lgkmcnt(4)
	global_store_dwordx4 v[16:17], v[12:15], off
	s_mov_b64 s[0:1], -1
	s_waitcnt lgkmcnt(0)
	global_store_dwordx4 v[16:17], v[4:7], off offset:256
	s_cbranch_vccnz .LBB0_2300
	s_andn2_b64 vcc, exec, s[38:39]
	s_cbranch_vccnz .LBB0_2299
	s_barrier
	s_branch .LBB0_2299

.LBB0_2797:
	v_lshl_add_u32 v144, s52, 8, v147
	s_lshl_b32 s0, s49, 8
	v_ashrrev_i32_e32 v145, 31, v144
	v_cvt_pk_bf16_f32 v124, v124, v125
	v_cvt_pk_bf16_f32 v125, v126, v127
	v_cvt_pk_bf16_f32 v126, v128, v129
	v_cvt_pk_bf16_f32 v127, v130, v131
	s_ashr_i32 s1, s0, 31
	v_lshlrev_b64 v[150:151], 11, v[144:145]
	ds_bpermute_b32 v124, v146, v124
	ds_bpermute_b32 v125, v146, v125
	ds_bpermute_b32 v126, v146, v126
	ds_bpermute_b32 v127, v146, v127
	v_lshl_add_u64 v[150:151], s[42:43], 0, v[150:151]
	s_lshl_b64 s[0:1], s[0:1], 1
	v_lshl_add_u64 v[128:129], v[150:151], 0, s[0:1]
	s_mov_b32 s49, s11
	v_lshl_add_u64 v[128:129], v[128:129], 0, s[48:49]
	v_lshl_add_u64 v[128:129], v[128:129], 0, v[2:3]
	v_cvt_pk_bf16_f32 v120, v120, v121
	v_cvt_pk_bf16_f32 v121, v122, v123
	v_cvt_pk_bf16_f32 v122, v116, v117
	v_cvt_pk_bf16_f32 v119, v118, v119
	ds_bpermute_b32 v116, v146, v120
	ds_bpermute_b32 v117, v146, v121
	ds_bpermute_b32 v118, v146, v122
	ds_bpermute_b32 v119, v146, v119
	s_waitcnt lgkmcnt(4)
	global_store_dwordx4 v[128:129], v[124:127], off
	s_and_b64 vcc, exec, s[34:35]
	v_cvt_pk_bf16_f32 v112, v112, v113
	v_cvt_pk_bf16_f32 v113, v114, v115
	v_cvt_pk_bf16_f32 v114, v108, v109
	v_cvt_pk_bf16_f32 v111, v110, v111
	ds_bpermute_b32 v108, v146, v112
	ds_bpermute_b32 v109, v146, v113
	ds_bpermute_b32 v110, v146, v114
	ds_bpermute_b32 v111, v146, v111
	s_waitcnt lgkmcnt(4)
	global_store_dwordx4 v[128:129], v[116:119], off offset:256
	s_nop 1
	v_or_b32_e32 v116, 16, v144
	v_ashrrev_i32_e32 v117, 31, v116
	v_lshlrev_b64 v[116:117], 11, v[116:117]
	v_lshl_add_u64 v[112:113], s[42:43], 0, v[116:117]
	v_lshl_add_u64 v[112:113], v[112:113], 0, s[0:1]
	v_lshl_add_u64 v[112:113], v[112:113], 0, s[48:49]
	v_lshl_add_u64 v[112:113], v[112:113], 0, v[2:3]
	v_cvt_pk_bf16_f32 v104, v104, v105
	v_cvt_pk_bf16_f32 v105, v106, v107
	v_cvt_pk_bf16_f32 v106, v100, v101
	v_cvt_pk_bf16_f32 v103, v102, v103
	ds_bpermute_b32 v100, v146, v104
	ds_bpermute_b32 v101, v146, v105
	ds_bpermute_b32 v102, v146, v106
	ds_bpermute_b32 v103, v146, v103
	s_waitcnt lgkmcnt(4)
	global_store_dwordx4 v[112:113], v[108:111], off
	v_cvt_pk_bf16_f32 v96, v96, v97
	v_cvt_pk_bf16_f32 v97, v98, v99
	v_cvt_pk_bf16_f32 v98, v92, v93
	v_cvt_pk_bf16_f32 v95, v94, v95
	ds_bpermute_b32 v92, v146, v96
	ds_bpermute_b32 v93, v146, v97
	ds_bpermute_b32 v94, v146, v98
	ds_bpermute_b32 v95, v146, v95
	s_waitcnt lgkmcnt(4)
	global_store_dwordx4 v[112:113], v[100:103], off offset:256
	s_nop 1
	v_or_b32_e32 v100, 32, v144
	v_ashrrev_i32_e32 v101, 31, v100
	v_lshlrev_b64 v[100:101], 11, v[100:101]
	v_lshl_add_u64 v[96:97], s[42:43], 0, v[100:101]
	v_lshl_add_u64 v[96:97], v[96:97], 0, s[0:1]
	v_lshl_add_u64 v[96:97], v[96:97], 0, s[48:49]
	v_lshl_add_u64 v[96:97], v[96:97], 0, v[2:3]
	v_cvt_pk_bf16_f32 v88, v88, v89
	v_cvt_pk_bf16_f32 v89, v90, v91
	v_cvt_pk_bf16_f32 v90, v84, v85
	v_cvt_pk_bf16_f32 v87, v86, v87
	ds_bpermute_b32 v84, v146, v88
	ds_bpermute_b32 v85, v146, v89
	ds_bpermute_b32 v86, v146, v90
	ds_bpermute_b32 v87, v146, v87
	s_waitcnt lgkmcnt(4)
	global_store_dwordx4 v[96:97], v[92:95], off
	v_cvt_pk_bf16_f32 v80, v80, v81
	v_cvt_pk_bf16_f32 v81, v82, v83
	v_cvt_pk_bf16_f32 v82, v76, v77
	v_cvt_pk_bf16_f32 v79, v78, v79
	ds_bpermute_b32 v76, v146, v80
	ds_bpermute_b32 v77, v146, v81
	ds_bpermute_b32 v78, v146, v82
	ds_bpermute_b32 v79, v146, v79
	s_waitcnt lgkmcnt(4)
	global_store_dwordx4 v[96:97], v[84:87], off offset:256
	s_nop 1
	v_or_b32_e32 v84, 48, v144
	v_ashrrev_i32_e32 v85, 31, v84
	v_lshlrev_b64 v[84:85], 11, v[84:85]
	v_lshl_add_u64 v[80:81], s[42:43], 0, v[84:85]
	v_lshl_add_u64 v[80:81], v[80:81], 0, s[0:1]
	v_lshl_add_u64 v[80:81], v[80:81], 0, s[48:49]
	v_lshl_add_u64 v[80:81], v[80:81], 0, v[2:3]
	v_cvt_pk_bf16_f32 v72, v72, v73
	v_cvt_pk_bf16_f32 v73, v74, v75
	v_cvt_pk_bf16_f32 v74, v68, v69
	v_cvt_pk_bf16_f32 v71, v70, v71
	ds_bpermute_b32 v68, v146, v72
	ds_bpermute_b32 v69, v146, v73
	ds_bpermute_b32 v70, v146, v74
	ds_bpermute_b32 v71, v146, v71
	s_waitcnt lgkmcnt(4)
	global_store_dwordx4 v[80:81], v[76:79], off
	v_cvt_pk_bf16_f32 v64, v64, v65
	v_cvt_pk_bf16_f32 v65, v66, v67
	v_cvt_pk_bf16_f32 v66, v60, v61
	v_cvt_pk_bf16_f32 v63, v62, v63
	ds_bpermute_b32 v60, v146, v64
	ds_bpermute_b32 v61, v146, v65
	ds_bpermute_b32 v62, v146, v66
	ds_bpermute_b32 v63, v146, v63
	s_waitcnt lgkmcnt(4)
	global_store_dwordx4 v[80:81], v[68:71], off offset:256
	s_nop 1
	v_add_u32_e32 v68, 0x80, v144
	v_ashrrev_i32_e32 v69, 31, v68
	v_lshlrev_b64 v[68:69], 11, v[68:69]
	v_lshl_add_u64 v[64:65], s[42:43], 0, v[68:69]
	v_lshl_add_u64 v[64:65], v[64:65], 0, s[0:1]
	v_lshl_add_u64 v[64:65], v[64:65], 0, s[48:49]
	v_lshl_add_u64 v[64:65], v[64:65], 0, v[2:3]
	v_cvt_pk_bf16_f32 v56, v56, v57
	v_cvt_pk_bf16_f32 v57, v58, v59
	v_cvt_pk_bf16_f32 v58, v52, v53
	v_cvt_pk_bf16_f32 v55, v54, v55
	ds_bpermute_b32 v52, v146, v56
	ds_bpermute_b32 v53, v146, v57
	ds_bpermute_b32 v54, v146, v58
	ds_bpermute_b32 v55, v146, v55
	s_waitcnt lgkmcnt(4)
	global_store_dwordx4 v[64:65], v[60:63], off
	v_cvt_pk_bf16_f32 v48, v48, v49
	v_cvt_pk_bf16_f32 v49, v50, v51
	v_cvt_pk_bf16_f32 v50, v44, v45
	v_cvt_pk_bf16_f32 v47, v46, v47
	ds_bpermute_b32 v44, v146, v48
	ds_bpermute_b32 v45, v146, v49
	ds_bpermute_b32 v46, v146, v50
	ds_bpermute_b32 v47, v146, v47
	s_waitcnt lgkmcnt(4)
	global_store_dwordx4 v[64:65], v[52:55], off offset:256
	s_nop 1
	v_add_u32_e32 v52, 0x90, v144
	v_ashrrev_i32_e32 v53, 31, v52
	v_lshlrev_b64 v[52:53], 11, v[52:53]
	v_lshl_add_u64 v[48:49], s[42:43], 0, v[52:53]
	v_lshl_add_u64 v[48:49], v[48:49], 0, s[0:1]
	v_lshl_add_u64 v[48:49], v[48:49], 0, s[48:49]
	v_lshl_add_u64 v[48:49], v[48:49], 0, v[2:3]
	v_cvt_pk_bf16_f32 v40, v40, v41
	v_cvt_pk_bf16_f32 v41, v42, v43
	v_cvt_pk_bf16_f32 v42, v36, v37
	v_cvt_pk_bf16_f32 v39, v38, v39
	ds_bpermute_b32 v36, v146, v40
	ds_bpermute_b32 v37, v146, v41
	ds_bpermute_b32 v38, v146, v42
	ds_bpermute_b32 v39, v146, v39
	s_waitcnt lgkmcnt(4)
	global_store_dwordx4 v[48:49], v[44:47], off
	v_cvt_pk_bf16_f32 v32, v32, v33
	v_cvt_pk_bf16_f32 v33, v34, v35
	v_cvt_pk_bf16_f32 v34, v28, v29
	v_cvt_pk_bf16_f32 v31, v30, v31
	ds_bpermute_b32 v28, v146, v32
	ds_bpermute_b32 v29, v146, v33
	ds_bpermute_b32 v30, v146, v34
	ds_bpermute_b32 v31, v146, v31
	s_waitcnt lgkmcnt(4)
	global_store_dwordx4 v[48:49], v[36:39], off offset:256
	s_nop 1
	v_add_u32_e32 v36, 0xa0, v144
	v_ashrrev_i32_e32 v37, 31, v36
	v_lshlrev_b64 v[36:37], 11, v[36:37]
	v_lshl_add_u64 v[32:33], s[42:43], 0, v[36:37]
	v_lshl_add_u64 v[32:33], v[32:33], 0, s[0:1]
	v_lshl_add_u64 v[32:33], v[32:33], 0, s[48:49]
	v_lshl_add_u64 v[32:33], v[32:33], 0, v[2:3]
	v_cvt_pk_bf16_f32 v24, v24, v25
	v_cvt_pk_bf16_f32 v25, v26, v27
	v_cvt_pk_bf16_f32 v26, v20, v21
	v_cvt_pk_bf16_f32 v23, v22, v23
	ds_bpermute_b32 v20, v146, v24
	ds_bpermute_b32 v21, v146, v25
	ds_bpermute_b32 v22, v146, v26
	ds_bpermute_b32 v23, v146, v23
	s_waitcnt lgkmcnt(4)
	global_store_dwordx4 v[32:33], v[28:31], off
	v_cvt_pk_bf16_f32 v16, v16, v17
	v_cvt_pk_bf16_f32 v17, v18, v19
	v_cvt_pk_bf16_f32 v18, v12, v13
	v_cvt_pk_bf16_f32 v15, v14, v15
	ds_bpermute_b32 v12, v146, v16
	ds_bpermute_b32 v13, v146, v17
	ds_bpermute_b32 v14, v146, v18
	ds_bpermute_b32 v15, v146, v15
	s_waitcnt lgkmcnt(4)
	global_store_dwordx4 v[32:33], v[20:23], off offset:256
	s_nop 1
	v_add_u32_e32 v20, 0xb0, v144
	v_ashrrev_i32_e32 v21, 31, v20
	v_lshlrev_b64 v[20:21], 11, v[20:21]
	v_lshl_add_u64 v[16:17], s[42:43], 0, v[20:21]
	v_lshl_add_u64 v[16:17], v[16:17], 0, s[0:1]
	v_lshl_add_u64 v[16:17], v[16:17], 0, s[48:49]
	v_lshl_add_u64 v[16:17], v[16:17], 0, v[2:3]
	v_cvt_pk_bf16_f32 v8, v8, v9
	v_cvt_pk_bf16_f32 v9, v10, v11
	v_cvt_pk_bf16_f32 v10, v4, v5
	v_cvt_pk_bf16_f32 v7, v6, v7
	ds_bpermute_b32 v4, v146, v8
	ds_bpermute_b32 v5, v146, v9
	ds_bpermute_b32 v6, v146, v10
	ds_bpermute_b32 v7, v146, v7
	s_waitcnt lgkmcnt(4)
	global_store_dwordx4 v[16:17], v[12:15], off
	s_mov_b64 s[0:1], -1
	s_waitcnt lgkmcnt(0)
	global_store_dwordx4 v[16:17], v[4:7], off offset:256
	s_cbranch_vccnz .LBB0_2781
	s_andn2_b64 vcc, exec, s[40:41]
	s_cbranch_vccnz .LBB0_2780
	s_barrier
	s_branch .LBB0_2780
